# router top-4: ds_bpermute max butterflies replaced by DPP reductions (exact) on top of P0 rows + P2 + conv waits
# speedup vs baseline: 1.0204x; 1.0000x over previous
; __device__ __forceinline__ float wave_max(float v) {
; #pragma unroll
;     for (int o = 1; o < 64; o <<= 1) v = fmaxf(v, __shfl_xor(v, o));
;     return v;
; }
; __device__ __forceinline__ void router_block(const Ctx& c, int blk, const float* __restrict__ h1, const float* __restrict__ g_ffn, const float* __restrict__ Wrt, const float* __restrict__ b_r, ...
;     ...
;         float tv[4];
; #pragma unroll
;         for (int k = 0; k < 4; ++k) {
;             const float mxv = wave_max(logit);
;             const unsigned long long mask = __ballot(logit == mxv);
;             const int idx = __ffsll((long long)mask) - 1;
;             tv[k] = mxv; se[r][k] = idx;
;             if (lane == idx) logit = -INFINITY;
;         }
;         float es = 0.f;
; #pragma unroll
;         for (int k = 0; k < 4; ++k) { sg[r][k] = expf(tv[k] - tv[0]); es += sg[r][k]; }
;         const float inv = 1.0f / es;
; #pragma unroll
;         for (int k = 0; k < 4; ++k) { sg[r][k] *= inv; sr[r][k] = 0u; if (lane == 0) sr[r][k] = __hip_atomic_fetch_add(&lhist[se[r][k]], 1u, __ATOMIC_RELAXED, __HIP_MEMORY_SCOPE_WORKGROUP); }
.LBB0_1237:
	s_or_b64 exec, exec, s[10:11]
	v_mov_b32_e32 v19, 0
	s_waitcnt lgkmcnt(0)
	v_max_f32_e32 v10, v2, v2
	s_nop 1
	v_max_f32_dpp v10, v10, v10 quad_perm:[1,0,3,2] row_mask:0xf bank_mask:0xf
	s_nop 1
	v_max_f32_dpp v10, v10, v10 quad_perm:[2,3,0,1] row_mask:0xf bank_mask:0xf
	s_nop 1
	v_max_f32_dpp v10, v10, v10 row_half_mirror row_mask:0xf bank_mask:0xf
	s_nop 1
	v_max_f32_dpp v10, v10, v10 row_mirror row_mask:0xf bank_mask:0xf
	s_nop 1
	v_max_f32_dpp v10, v10, v10 row_bcast:15 row_mask:0xa bank_mask:0xf
	s_nop 1
	v_max_f32_dpp v10, v10, v10 row_bcast:31 row_mask:0xc bank_mask:0xf
	s_nop 1
	v_readlane_b32 s98, v10, 63
	s_nop 1
	v_mov_b32_e32 v10, s98
	v_cmp_eq_f32_e32 vcc, v2, v10
	s_ff1_i32_b64 s10, vcc
	s_cmp_lg_u64 vcc, 0
	s_cselect_b32 s25, s10, -1
	v_cmp_ne_u32_e32 vcc, s25, v1
	s_nop 1
	v_cndmask_b32_e32 v2, v233, v2, vcc
	s_waitcnt lgkmcnt(0)
	v_max_f32_e32 v21, v2, v2
	s_nop 1
	v_max_f32_dpp v21, v21, v21 quad_perm:[1,0,3,2] row_mask:0xf bank_mask:0xf
	s_nop 1
	v_max_f32_dpp v21, v21, v21 quad_perm:[2,3,0,1] row_mask:0xf bank_mask:0xf
	s_nop 1
	v_max_f32_dpp v21, v21, v21 row_half_mirror row_mask:0xf bank_mask:0xf
	s_nop 1
	v_max_f32_dpp v21, v21, v21 row_mirror row_mask:0xf bank_mask:0xf
	s_nop 1
	v_max_f32_dpp v21, v21, v21 row_bcast:15 row_mask:0xa bank_mask:0xf
	s_nop 1
	v_max_f32_dpp v21, v21, v21 row_bcast:31 row_mask:0xc bank_mask:0xf
	s_nop 1
	v_readlane_b32 s98, v21, 63
	s_nop 1
	v_mov_b32_e32 v21, s98
	v_cmp_eq_f32_e32 vcc, v2, v21
	s_ff1_i32_b64 s10, vcc
	s_cmp_lg_u64 vcc, 0
	s_cselect_b32 s15, s10, -1
	v_cmp_ne_u32_e32 vcc, s15, v1
	s_nop 1
	v_cndmask_b32_e32 v2, v233, v2, vcc
	s_waitcnt lgkmcnt(0)
	v_max_f32_e32 v20, v2, v2
	s_nop 1
	v_max_f32_dpp v20, v20, v20 quad_perm:[1,0,3,2] row_mask:0xf bank_mask:0xf
	s_nop 1
	v_max_f32_dpp v20, v20, v20 quad_perm:[2,3,0,1] row_mask:0xf bank_mask:0xf
	s_nop 1
	v_max_f32_dpp v20, v20, v20 row_half_mirror row_mask:0xf bank_mask:0xf
	s_nop 1
	v_max_f32_dpp v20, v20, v20 row_mirror row_mask:0xf bank_mask:0xf
	s_nop 1
	v_max_f32_dpp v20, v20, v20 row_bcast:15 row_mask:0xa bank_mask:0xf
	s_nop 1
	v_max_f32_dpp v20, v20, v20 row_bcast:31 row_mask:0xc bank_mask:0xf
	s_nop 1
	v_readlane_b32 s98, v20, 63
	s_nop 1
	v_mov_b32_e32 v20, s98
	v_cmp_eq_f32_e32 vcc, v2, v20
	s_ff1_i32_b64 s10, vcc
	s_cmp_lg_u64 vcc, 0
	s_cselect_b32 s18, s10, -1
	v_cmp_ne_u32_e32 vcc, s18, v1
	s_nop 1
	v_cndmask_b32_e32 v2, v233, v2, vcc
	s_waitcnt lgkmcnt(0)
	v_max_f32_e32 v11, v2, v2
	s_nop 1
	v_max_f32_dpp v11, v11, v11 quad_perm:[1,0,3,2] row_mask:0xf bank_mask:0xf
	s_nop 1
	v_max_f32_dpp v11, v11, v11 quad_perm:[2,3,0,1] row_mask:0xf bank_mask:0xf
	s_nop 1
	v_max_f32_dpp v11, v11, v11 row_half_mirror row_mask:0xf bank_mask:0xf
	s_nop 1
	v_max_f32_dpp v11, v11, v11 row_mirror row_mask:0xf bank_mask:0xf
	s_nop 1
	v_max_f32_dpp v11, v11, v11 row_bcast:15 row_mask:0xa bank_mask:0xf
	s_nop 1
	v_max_f32_dpp v11, v11, v11 row_bcast:31 row_mask:0xc bank_mask:0xf
	s_nop 1
	v_readlane_b32 s98, v11, 63
	s_nop 1
	v_mov_b32_e32 v11, s98
	v_cmp_eq_f32_e32 vcc, v2, v11
	s_and_saveexec_b64 s[46:47], s[4:5]
	s_cbranch_execz .LBB0_1242
	s_mov_b64 s[50:51], exec
	v_mbcnt_lo_u32_b32 v2, s50, 0
	v_mbcnt_hi_u32_b32 v2, s51, v2
	v_cmp_eq_u32_e64 s[10:11], 0, v2
	s_and_saveexec_b64 s[48:49], s[10:11]
	s_cbranch_execz .LBB0_1240
	s_lshl_b32 s10, s25, 2
	s_add_i32 s10, s10, 0
	s_add_i32 s10, s10, 0x20480
	s_bcnt1_i32_b64 s11, s[50:51]
	v_mov_b32_e32 v3, s10
	v_mov_b32_e32 v4, s11
	ds_add_rtn_u32 v3, v3, v4

; __device__ __forceinline__ float wave_max(float v) {
; #pragma unroll
;     for (int o = 1; o < 64; o <<= 1) v = fmaxf(v, __shfl_xor(v, o));
;     return v;
; }
; __device__ __forceinline__ void router_block(const Ctx& c, int blk, const float* __restrict__ h1, const float* __restrict__ g_ffn, const float* __restrict__ Wrt, const float* __restrict__ b_r, ...
;     ...
;         float tv[4];
; #pragma unroll
;         for (int k = 0; k < 4; ++k) {
;             const float mxv = wave_max(logit);
;             const unsigned long long mask = __ballot(logit == mxv);
;             const int idx = __ffsll((long long)mask) - 1;
;             tv[k] = mxv; se[r][k] = idx;
;             if (lane == idx) logit = -INFINITY;
;         }
;         float es = 0.f;
; #pragma unroll
;         for (int k = 0; k < 4; ++k) { sg[r][k] = expf(tv[k] - tv[0]); es += sg[r][k]; }
;         const float inv = 1.0f / es;
; #pragma unroll
;         for (int k = 0; k < 4; ++k) { sg[r][k] *= inv; sr[r][k] = 0u; if (lane == 0) sr[r][k] = __hip_atomic_fetch_add(&lhist[se[r][k]], 1u, __ATOMIC_RELAXED, __HIP_MEMORY_SCOPE_WORKGROUP); }
.LBB0_1255:
	s_or_b64 exec, exec, s[10:11]
	v_mov_b32_e32 v25, 0
	s_waitcnt lgkmcnt(0)
	v_max_f32_e32 v6, v2, v2
	s_nop 1
	v_max_f32_dpp v6, v6, v6 quad_perm:[1,0,3,2] row_mask:0xf bank_mask:0xf
	s_nop 1
	v_max_f32_dpp v6, v6, v6 quad_perm:[2,3,0,1] row_mask:0xf bank_mask:0xf
	s_nop 1
	v_max_f32_dpp v6, v6, v6 row_half_mirror row_mask:0xf bank_mask:0xf
	s_nop 1
	v_max_f32_dpp v6, v6, v6 row_mirror row_mask:0xf bank_mask:0xf
	s_nop 1
	v_max_f32_dpp v6, v6, v6 row_bcast:15 row_mask:0xa bank_mask:0xf
	s_nop 1
	v_max_f32_dpp v6, v6, v6 row_bcast:31 row_mask:0xc bank_mask:0xf
	s_nop 1
	v_readlane_b32 s98, v6, 63
	s_nop 1
	v_mov_b32_e32 v6, s98
	v_cmp_eq_f32_e32 vcc, v2, v6
	s_ff1_i32_b64 s10, vcc
	s_cmp_lg_u64 vcc, 0
	s_cselect_b32 s45, s10, -1
	v_cmp_ne_u32_e32 vcc, s45, v1
	s_nop 1
	v_cndmask_b32_e32 v2, v233, v2, vcc
	s_waitcnt lgkmcnt(0)
	v_max_f32_e32 v13, v2, v2
	s_nop 1
	v_max_f32_dpp v13, v13, v13 quad_perm:[1,0,3,2] row_mask:0xf bank_mask:0xf
	s_nop 1
	v_max_f32_dpp v13, v13, v13 quad_perm:[2,3,0,1] row_mask:0xf bank_mask:0xf
	s_nop 1
	v_max_f32_dpp v13, v13, v13 row_half_mirror row_mask:0xf bank_mask:0xf
	s_nop 1
	v_max_f32_dpp v13, v13, v13 row_mirror row_mask:0xf bank_mask:0xf
	s_nop 1
	v_max_f32_dpp v13, v13, v13 row_bcast:15 row_mask:0xa bank_mask:0xf
	s_nop 1
	v_max_f32_dpp v13, v13, v13 row_bcast:31 row_mask:0xc bank_mask:0xf
	s_nop 1
	v_readlane_b32 s98, v13, 63
	s_nop 1
	v_mov_b32_e32 v13, s98
	v_cmp_eq_f32_e32 vcc, v2, v13
	s_ff1_i32_b64 s10, vcc
	s_cmp_lg_u64 vcc, 0
	s_cselect_b32 s19, s10, -1
	v_cmp_ne_u32_e32 vcc, s19, v1
	s_nop 1
	v_cndmask_b32_e32 v2, v233, v2, vcc
	s_waitcnt lgkmcnt(0)
	v_max_f32_e32 v12, v2, v2
	s_nop 1
	v_max_f32_dpp v12, v12, v12 quad_perm:[1,0,3,2] row_mask:0xf bank_mask:0xf
	s_nop 1
	v_max_f32_dpp v12, v12, v12 quad_perm:[2,3,0,1] row_mask:0xf bank_mask:0xf
	s_nop 1
	v_max_f32_dpp v12, v12, v12 row_half_mirror row_mask:0xf bank_mask:0xf
	s_nop 1
	v_max_f32_dpp v12, v12, v12 row_mirror row_mask:0xf bank_mask:0xf
	s_nop 1
	v_max_f32_dpp v12, v12, v12 row_bcast:15 row_mask:0xa bank_mask:0xf
	s_nop 1
	v_max_f32_dpp v12, v12, v12 row_bcast:31 row_mask:0xc bank_mask:0xf
	s_nop 1
	v_readlane_b32 s98, v12, 63
	s_nop 1
	v_mov_b32_e32 v12, s98
	v_cmp_eq_f32_e32 vcc, v2, v12
	s_ff1_i32_b64 s10, vcc
	s_cmp_lg_u64 vcc, 0
	s_cselect_b32 s24, s10, -1
	v_cmp_ne_u32_e32 vcc, s24, v1
	s_nop 1
	v_cndmask_b32_e32 v2, v233, v2, vcc
	s_waitcnt lgkmcnt(0)
	v_max_f32_e32 v7, v2, v2
	s_nop 1
	v_max_f32_dpp v7, v7, v7 quad_perm:[1,0,3,2] row_mask:0xf bank_mask:0xf
	s_nop 1
	v_max_f32_dpp v7, v7, v7 quad_perm:[2,3,0,1] row_mask:0xf bank_mask:0xf
	s_nop 1
	v_max_f32_dpp v7, v7, v7 row_half_mirror row_mask:0xf bank_mask:0xf
	s_nop 1
	v_max_f32_dpp v7, v7, v7 row_mirror row_mask:0xf bank_mask:0xf
	s_nop 1
	v_max_f32_dpp v7, v7, v7 row_bcast:15 row_mask:0xa bank_mask:0xf
	s_nop 1
	v_max_f32_dpp v7, v7, v7 row_bcast:31 row_mask:0xc bank_mask:0xf
	s_nop 1
	v_readlane_b32 s98, v7, 63
	s_nop 1
	v_mov_b32_e32 v7, s98
	v_cmp_eq_f32_e32 vcc, v2, v7
	s_and_saveexec_b64 s[46:47], s[4:5]
	s_cbranch_execz .LBB0_1260
	s_mov_b64 s[50:51], exec
	v_mbcnt_lo_u32_b32 v2, s50, 0
	v_mbcnt_hi_u32_b32 v2, s51, v2
	v_cmp_eq_u32_e64 s[10:11], 0, v2
	s_and_saveexec_b64 s[48:49], s[10:11]
	s_cbranch_execz .LBB0_1258
	s_lshl_b32 s10, s45, 2
	s_add_i32 s10, s10, 0
	s_add_i32 s10, s10, 0x20480
	s_bcnt1_i32_b64 s11, s[50:51]
	v_mov_b32_e32 v3, s10
	v_mov_b32_e32 v4, s11
	ds_add_rtn_u32 v3, v3, v4

; __device__ __forceinline__ float wave_max(float v) {
; #pragma unroll
;     for (int o = 1; o < 64; o <<= 1) v = fmaxf(v, __shfl_xor(v, o));
;     return v;
; }
; __device__ __forceinline__ void router_block(const Ctx& c, int blk, const float* __restrict__ h1, const float* __restrict__ g_ffn, const float* __restrict__ Wrt, const float* __restrict__ b_r, ...
;     ...
;         float tv[4];
; #pragma unroll
;         for (int k = 0; k < 4; ++k) {
;             const float mxv = wave_max(logit);
;             const unsigned long long mask = __ballot(logit == mxv);
;             const int idx = __ffsll((long long)mask) - 1;
;             tv[k] = mxv; se[r][k] = idx;
;             if (lane == idx) logit = -INFINITY;
;         }
;         float es = 0.f;
; #pragma unroll
;         for (int k = 0; k < 4; ++k) { sg[r][k] = expf(tv[k] - tv[0]); es += sg[r][k]; }
;         const float inv = 1.0f / es;
; #pragma unroll
;         for (int k = 0; k < 4; ++k) { sg[r][k] *= inv; sr[r][k] = 0u; if (lane == 0) sr[r][k] = __hip_atomic_fetch_add(&lhist[se[r][k]], 1u, __ATOMIC_RELAXED, __HIP_MEMORY_SCOPE_WORKGROUP); }
.LBB0_1273:
	s_or_b64 exec, exec, s[10:11]
	v_mov_b32_e32 v29, 0
	s_waitcnt lgkmcnt(0)
	v_max_f32_e32 v2, v3, v3
	s_nop 1
	v_max_f32_dpp v2, v2, v2 quad_perm:[1,0,3,2] row_mask:0xf bank_mask:0xf
	s_nop 1
	v_max_f32_dpp v2, v2, v2 quad_perm:[2,3,0,1] row_mask:0xf bank_mask:0xf
	s_nop 1
	v_max_f32_dpp v2, v2, v2 row_half_mirror row_mask:0xf bank_mask:0xf
	s_nop 1
	v_max_f32_dpp v2, v2, v2 row_mirror row_mask:0xf bank_mask:0xf
	s_nop 1
	v_max_f32_dpp v2, v2, v2 row_bcast:15 row_mask:0xa bank_mask:0xf
	s_nop 1
	v_max_f32_dpp v2, v2, v2 row_bcast:31 row_mask:0xc bank_mask:0xf
	s_nop 1
	v_readlane_b32 s98, v2, 63
	s_nop 1
	v_mov_b32_e32 v2, s98
	v_cmp_eq_f32_e32 vcc, v3, v2
	s_ff1_i32_b64 s10, vcc
	s_cmp_lg_u64 vcc, 0
	s_cselect_b32 s82, s10, -1
	v_cmp_ne_u32_e32 vcc, s82, v1
	s_nop 1
	v_cndmask_b32_e32 v3, v233, v3, vcc
	s_waitcnt lgkmcnt(0)
	v_max_f32_e32 v9, v3, v3
	s_nop 1
	v_max_f32_dpp v9, v9, v9 quad_perm:[1,0,3,2] row_mask:0xf bank_mask:0xf
	s_nop 1
	v_max_f32_dpp v9, v9, v9 quad_perm:[2,3,0,1] row_mask:0xf bank_mask:0xf
	s_nop 1
	v_max_f32_dpp v9, v9, v9 row_half_mirror row_mask:0xf bank_mask:0xf
	s_nop 1
	v_max_f32_dpp v9, v9, v9 row_mirror row_mask:0xf bank_mask:0xf
	s_nop 1
	v_max_f32_dpp v9, v9, v9 row_bcast:15 row_mask:0xa bank_mask:0xf
	s_nop 1
	v_max_f32_dpp v9, v9, v9 row_bcast:31 row_mask:0xc bank_mask:0xf
	s_nop 1
	v_readlane_b32 s98, v9, 63
	s_nop 1
	v_mov_b32_e32 v9, s98
	v_cmp_eq_f32_e32 vcc, v3, v9
	s_ff1_i32_b64 s10, vcc
	s_cmp_lg_u64 vcc, 0
	s_cselect_b32 s27, s10, -1
	v_cmp_ne_u32_e32 vcc, s27, v1
	s_nop 1
	v_cndmask_b32_e32 v3, v233, v3, vcc
	s_waitcnt lgkmcnt(0)
	v_max_f32_e32 v8, v3, v3
	s_nop 1
	v_max_f32_dpp v8, v8, v8 quad_perm:[1,0,3,2] row_mask:0xf bank_mask:0xf
	s_nop 1
	v_max_f32_dpp v8, v8, v8 quad_perm:[2,3,0,1] row_mask:0xf bank_mask:0xf
	s_nop 1
	v_max_f32_dpp v8, v8, v8 row_half_mirror row_mask:0xf bank_mask:0xf
	s_nop 1
	v_max_f32_dpp v8, v8, v8 row_mirror row_mask:0xf bank_mask:0xf
	s_nop 1
	v_max_f32_dpp v8, v8, v8 row_bcast:15 row_mask:0xa bank_mask:0xf
	s_nop 1
	v_max_f32_dpp v8, v8, v8 row_bcast:31 row_mask:0xc bank_mask:0xf
	s_nop 1
	v_readlane_b32 s98, v8, 63
	s_nop 1
	v_mov_b32_e32 v8, s98
	v_cmp_eq_f32_e32 vcc, v3, v8
	s_ff1_i32_b64 s10, vcc
	s_cmp_lg_u64 vcc, 0
	s_cselect_b32 s41, s10, -1
	v_cmp_ne_u32_e32 vcc, s41, v1
	s_nop 1
	v_cndmask_b32_e32 v4, v233, v3, vcc
	s_waitcnt lgkmcnt(0)
	v_max_f32_e32 v3, v4, v4
	s_nop 1
	v_max_f32_dpp v3, v3, v3 quad_perm:[1,0,3,2] row_mask:0xf bank_mask:0xf
	s_nop 1
	v_max_f32_dpp v3, v3, v3 quad_perm:[2,3,0,1] row_mask:0xf bank_mask:0xf
	s_nop 1
	v_max_f32_dpp v3, v3, v3 row_half_mirror row_mask:0xf bank_mask:0xf
	s_nop 1
	v_max_f32_dpp v3, v3, v3 row_mirror row_mask:0xf bank_mask:0xf
	s_nop 1
	v_max_f32_dpp v3, v3, v3 row_bcast:15 row_mask:0xa bank_mask:0xf
	s_nop 1
	v_max_f32_dpp v3, v3, v3 row_bcast:31 row_mask:0xc bank_mask:0xf
	s_nop 1
	v_readlane_b32 s98, v3, 63
	s_nop 1
	v_mov_b32_e32 v3, s98
	v_cmp_eq_f32_e32 vcc, v4, v3
	s_and_saveexec_b64 s[46:47], s[4:5]
	s_cbranch_execz .LBB0_1278
	s_mov_b64 s[50:51], exec
	v_mbcnt_lo_u32_b32 v4, s50, 0
	v_mbcnt_hi_u32_b32 v4, s51, v4
	v_cmp_eq_u32_e64 s[10:11], 0, v4
	s_and_saveexec_b64 s[48:49], s[10:11]
	s_cbranch_execz .LBB0_1276
	s_lshl_b32 s10, s82, 2
	s_add_i32 s10, s10, 0
	s_add_i32 s10, s10, 0x20480
	s_bcnt1_i32_b64 s11, s[50:51]
	v_mov_b32_e32 v5, s10
	v_mov_b32_e32 v14, s11
	ds_add_rtn_u32 v5, v5, v14

; __device__ __forceinline__ float wave_max(float v) {
; #pragma unroll
;     for (int o = 1; o < 64; o <<= 1) v = fmaxf(v, __shfl_xor(v, o));
;     return v;
; }
; __device__ __forceinline__ void router_block(const Ctx& c, int blk, const float* __restrict__ h1, const float* __restrict__ g_ffn, const float* __restrict__ Wrt, const float* __restrict__ b_r, ...
;     ...
;         float tv[4];
; #pragma unroll
;         for (int k = 0; k < 4; ++k) {
;             const float mxv = wave_max(logit);
;             const unsigned long long mask = __ballot(logit == mxv);
;             const int idx = __ffsll((long long)mask) - 1;
;             tv[k] = mxv; se[r][k] = idx;
;             if (lane == idx) logit = -INFINITY;
;         }
;         float es = 0.f;
; #pragma unroll
;         for (int k = 0; k < 4; ++k) { sg[r][k] = expf(tv[k] - tv[0]); es += sg[r][k]; }
;         const float inv = 1.0f / es;
; #pragma unroll
;         for (int k = 0; k < 4; ++k) { sg[r][k] *= inv; sr[r][k] = 0u; if (lane == 0) sr[r][k] = __hip_atomic_fetch_add(&lhist[se[r][k]], 1u, __ATOMIC_RELAXED, __HIP_MEMORY_SCOPE_WORKGROUP); }
.LBB0_1291:
	s_or_b64 exec, exec, s[10:11]
	v_mov_b32_e32 v33, 0
	s_waitcnt lgkmcnt(0)
	v_max_f32_e32 v4, v5, v5
	s_nop 1
	v_max_f32_dpp v4, v4, v4 quad_perm:[1,0,3,2] row_mask:0xf bank_mask:0xf
	s_nop 1
	v_max_f32_dpp v4, v4, v4 quad_perm:[2,3,0,1] row_mask:0xf bank_mask:0xf
	s_nop 1
	v_max_f32_dpp v4, v4, v4 row_half_mirror row_mask:0xf bank_mask:0xf
	s_nop 1
	v_max_f32_dpp v4, v4, v4 row_mirror row_mask:0xf bank_mask:0xf
	s_nop 1
	v_max_f32_dpp v4, v4, v4 row_bcast:15 row_mask:0xa bank_mask:0xf
	s_nop 1
	v_max_f32_dpp v4, v4, v4 row_bcast:31 row_mask:0xc bank_mask:0xf
	s_nop 1
	v_readlane_b32 s98, v4, 63
	s_nop 1
	v_mov_b32_e32 v4, s98
	v_cmp_eq_f32_e32 vcc, v5, v4
	s_ff1_i32_b64 s10, vcc
	s_cmp_lg_u64 vcc, 0
	s_cselect_b32 s85, s10, -1
	v_cmp_ne_u32_e32 vcc, s85, v1
	s_nop 1
	v_cndmask_b32_e32 v5, v233, v5, vcc
	s_waitcnt lgkmcnt(0)
	v_max_f32_e32 v15, v5, v5
	s_nop 1
	v_max_f32_dpp v15, v15, v15 quad_perm:[1,0,3,2] row_mask:0xf bank_mask:0xf
	s_nop 1
	v_max_f32_dpp v15, v15, v15 quad_perm:[2,3,0,1] row_mask:0xf bank_mask:0xf
	s_nop 1
	v_max_f32_dpp v15, v15, v15 row_half_mirror row_mask:0xf bank_mask:0xf
	s_nop 1
	v_max_f32_dpp v15, v15, v15 row_mirror row_mask:0xf bank_mask:0xf
	s_nop 1
	v_max_f32_dpp v15, v15, v15 row_bcast:15 row_mask:0xa bank_mask:0xf
	s_nop 1
	v_max_f32_dpp v15, v15, v15 row_bcast:31 row_mask:0xc bank_mask:0xf
	s_nop 1
	v_readlane_b32 s98, v15, 63
	s_nop 1
	v_mov_b32_e32 v15, s98
	v_cmp_eq_f32_e32 vcc, v5, v15
	s_ff1_i32_b64 s10, vcc
	s_cmp_lg_u64 vcc, 0
	s_cselect_b32 s80, s10, -1
	v_cmp_ne_u32_e32 vcc, s80, v1
	s_nop 1
	v_cndmask_b32_e32 v5, v233, v5, vcc
	s_waitcnt lgkmcnt(0)
	v_max_f32_e32 v14, v5, v5
	s_nop 1
	v_max_f32_dpp v14, v14, v14 quad_perm:[1,0,3,2] row_mask:0xf bank_mask:0xf
	s_nop 1
	v_max_f32_dpp v14, v14, v14 quad_perm:[2,3,0,1] row_mask:0xf bank_mask:0xf
	s_nop 1
	v_max_f32_dpp v14, v14, v14 row_half_mirror row_mask:0xf bank_mask:0xf
	s_nop 1
	v_max_f32_dpp v14, v14, v14 row_mirror row_mask:0xf bank_mask:0xf
	s_nop 1
	v_max_f32_dpp v14, v14, v14 row_bcast:15 row_mask:0xa bank_mask:0xf
	s_nop 1
	v_max_f32_dpp v14, v14, v14 row_bcast:31 row_mask:0xc bank_mask:0xf
	s_nop 1
	v_readlane_b32 s98, v14, 63
	s_nop 1
	v_mov_b32_e32 v14, s98
	v_cmp_eq_f32_e32 vcc, v5, v14
	s_ff1_i32_b64 s10, vcc
	s_cmp_lg_u64 vcc, 0
	s_cselect_b32 s81, s10, -1
	v_cmp_ne_u32_e32 vcc, s81, v1
	s_nop 1
	v_cndmask_b32_e32 v30, v233, v5, vcc
	s_waitcnt lgkmcnt(0)
	v_max_f32_e32 v5, v30, v30
	s_nop 1
	v_max_f32_dpp v5, v5, v5 quad_perm:[1,0,3,2] row_mask:0xf bank_mask:0xf
	s_nop 1
	v_max_f32_dpp v5, v5, v5 quad_perm:[2,3,0,1] row_mask:0xf bank_mask:0xf
	s_nop 1
	v_max_f32_dpp v5, v5, v5 row_half_mirror row_mask:0xf bank_mask:0xf
	s_nop 1
	v_max_f32_dpp v5, v5, v5 row_mirror row_mask:0xf bank_mask:0xf
	s_nop 1
	v_max_f32_dpp v5, v5, v5 row_bcast:15 row_mask:0xa bank_mask:0xf
	s_nop 1
	v_max_f32_dpp v5, v5, v5 row_bcast:31 row_mask:0xc bank_mask:0xf
	s_nop 1
	v_readlane_b32 s98, v5, 63
	s_nop 1
	v_mov_b32_e32 v5, s98
	v_cmp_eq_f32_e32 vcc, v30, v5
	s_and_saveexec_b64 s[46:47], s[4:5]
	s_cbranch_execz .LBB0_1296
	s_mov_b64 s[50:51], exec
	v_mbcnt_lo_u32_b32 v30, s50, 0
	v_mbcnt_hi_u32_b32 v30, s51, v30
	v_cmp_eq_u32_e64 s[10:11], 0, v30
	s_and_saveexec_b64 s[48:49], s[10:11]
	s_cbranch_execz .LBB0_1294
	s_lshl_b32 s10, s85, 2
	s_add_i32 s10, s10, 0
	s_add_i32 s10, s10, 0x20480
	s_bcnt1_i32_b64 s11, s[50:51]
	v_mov_b32_e32 v31, s10
	v_mov_b32_e32 v32, s11
	ds_add_rtn_u32 v31, v31, v32

; __global__ void __launch_bounds__(NWAVES * 64, 2) mk_fwd(Args a) {
	.amdhsa_kernel _Z6mk_fwd4Args
		.amdhsa_group_segment_fixed_size 0
		.amdhsa_private_segment_fixed_size 0
		.amdhsa_kernarg_size 440
		.amdhsa_user_sgpr_count 2
		.amdhsa_user_sgpr_dispatch_ptr 0
		.amdhsa_user_sgpr_queue_ptr 0
		.amdhsa_user_sgpr_kernarg_segment_ptr 1
		.amdhsa_user_sgpr_dispatch_id 0
		.amdhsa_user_sgpr_kernarg_preload_length 0
		.amdhsa_user_sgpr_kernarg_preload_offset 0
		.amdhsa_user_sgpr_private_segment_size 0
		.amdhsa_uses_dynamic_stack 0
		.amdhsa_enable_private_segment 0
		.amdhsa_system_sgpr_workgroup_id_x 1
		.amdhsa_system_sgpr_workgroup_id_y 0
		.amdhsa_system_sgpr_workgroup_id_z 0
		.amdhsa_system_sgpr_workgroup_info 0
		.amdhsa_system_vgpr_workitem_id 0
		.amdhsa_next_free_vgpr 253
		.amdhsa_next_free_sgpr 99
		.amdhsa_accum_offset 256
		.amdhsa_reserve_vcc 1
		.amdhsa_float_round_mode_32 0
		.amdhsa_float_round_mode_16_64 0
		.amdhsa_float_denorm_mode_32 3
		.amdhsa_float_denorm_mode_16_64 3
		.amdhsa_dx10_clamp 1
		.amdhsa_ieee_mode 1
		.amdhsa_fp16_overflow 0
		.amdhsa_tg_split 0
		.amdhsa_exception_fp_ieee_invalid_op 0
		.amdhsa_exception_fp_denorm_src 0
		.amdhsa_exception_fp_ieee_div_zero 0
		.amdhsa_exception_fp_ieee_overflow 0
		.amdhsa_exception_fp_ieee_underflow 0
		.amdhsa_exception_fp_ieee_inexact 0
		.amdhsa_exception_int_div_zero 0
	.end_amdhsa_kernel

; __global__ void __launch_bounds__(NWAVES * 64, 2) mk_fwd(Args a) {
amdhsa.kernels:
  - .agpr_count:     0
    .args:
      - .offset:         0
        .size:           184
        .value_kind:     by_value
      - .offset:         184
        .size:           4
        .value_kind:     hidden_block_count_x
      - .offset:         188
        .size:           4
        .value_kind:     hidden_block_count_y
      - .offset:         192
        .size:           4
        .value_kind:     hidden_block_count_z
      - .offset:         196
        .size:           2
        .value_kind:     hidden_group_size_x
      - .offset:         198
        .size:           2
        .value_kind:     hidden_group_size_y
      - .offset:         200
        .size:           2
        .value_kind:     hidden_group_size_z
      - .offset:         202
        .size:           2
        .value_kind:     hidden_remainder_x
      - .offset:         204
        .size:           2
        .value_kind:     hidden_remainder_y
      - .offset:         206
        .size:           2
        .value_kind:     hidden_remainder_z
      - .offset:         224
        .size:           8
        .value_kind:     hidden_global_offset_x
      - .offset:         232
        .size:           8
        .value_kind:     hidden_global_offset_y
      - .offset:         240
        .size:           8
        .value_kind:     hidden_global_offset_z
      - .offset:         248
        .size:           2
        .value_kind:     hidden_grid_dims
      - .offset:         304
        .size:           4
        .value_kind:     hidden_dynamic_lds_size
    .group_segment_fixed_size: 0
    .kernarg_segment_align: 8
    .kernarg_segment_size: 440
    .language:       OpenCL C
    .language_version:
      - 2
      - 0
    .max_flat_workgroup_size: 512
    .name:           _Z6mk_fwd4Args
    .private_segment_fixed_size: 0
    .sgpr_count:     105
    .sgpr_spill_count: 21
    .symbol:         _Z6mk_fwd4Args.kd
    .uniform_work_group_size: 1
    .uses_dynamic_stack: false
    .vgpr_count:     253
    .vgpr_spill_count: 0
    .wavefront_size: 64
